# S.next search vectorized (wave-parallel compare+popcount); P8 K-loop: LDS-DMA stage issues moved into MFMA blocks, mid-segment lgkmcnt(0) dropped
# speedup vs baseline: 1.0106x; 1.0106x over previous
; #define PG8_LAS __attribute__((address_space(3)))
; __device__ __forceinline__ unsigned long long rt() { return __builtin_amdgcn_s_memrealtime(); }
;     __device__ __forceinline__ bool next(int i, Unit& u) const {
;         const PG8_LAS int* TH = TS + 33;
;         const int U = i * G + v; const int FT = __builtin_amdgcn_readfirstlane(TS[32] * nN), total = FT + __builtin_amdgcn_readfirstlane(TH[32] * nN); if (U >= total) return false;
;         int e = 0, pn, rt;
;         if (U < FT) {
; #pragma unroll 1
;             for (int j = 1; j < 32; ++j) e += (TS[j] * nN <= U) ? 1 : 0;
;             const int t0 = TS[e], nt = TS[e + 1] - t0, loc = U - t0 * nN; pn = loc / nt; rt = loc - pn * nt;
;         } else { const int U2 = U - FT;
; #pragma unroll 1
;             for (int j = 1; j < 32; ++j) e += (TH[j] * nN <= U2) ? 1 : 0;
;             pn = U2 - TH[e] * nN; rt = TS[e + 1] - TS[e]; }
;         const int left = CN[e] - rt * BM;
;         u.pm = __builtin_amdgcn_readfirstlane(e * 32 + rt); u.pn = __builtin_amdgcn_readfirstlane(e * nN + pn); u.e = __builtin_amdgcn_readfirstlane(e); u.cn = __builtin_amdgcn_readfirstlane(pn);
;         u.rows = __builtin_amdgcn_readfirstlane(left < BM ? left : BM); u.boff = (long)u.e * b_estride + (long)u.cn * b_cnstep; return true;
.LBB0_766:
	ds_read_b32 v2, v1
	ds_read_b32 v3, v207
	s_add_i32 s58, s58, 1
	s_lshl_b32 s2, s58, 8
	s_add_i32 s23, s2, s29
	s_waitcnt lgkmcnt(0)
	v_readfirstlane_b32 s2, v2
	v_readfirstlane_b32 s3, v3
	s_add_i32 s3, s3, s2
	s_lshl_b32 s3, s3, 4
	s_cmp_lt_i32 s23, s3
	s_cselect_b64 s[20:21], -1, 0
	s_cmp_ge_i32 s23, s3
	s_cbranch_scc1 .LBB0_780
	s_lshl_b32 s2, s2, 4
	s_cmp_ge_i32 s23, s2
	s_cbranch_scc0 .LBB0_773
	s_sub_i32 s22, s23, s2
	s_mov_b32 s24, s22
	s_mov_b32 s25, 0
	s_mov_b32 s26, 0
	s_mov_b32 s27, 0
	s_mov_b64 s[2:3], exec
	s_mov_b64 exec, -1
	v_and_b32_e32 v2, 63, v0
	v_lshlrev_b32_e32 v2, 2, v2
	v_add_u32_e32 v2, 0x20484, v2
	ds_read_b32 v2, v2
	s_waitcnt lgkmcnt(0)
	v_lshlrev_b32_e32 v2, 4, v2
	v_cmp_ge_i32_e32 vcc, s22, v2
	s_mov_b64 exec, s[2:3]
	s_mov_b32 s2, 0xfffffffe
	s_mov_b32 s3, 0
	s_and_b64 vcc, vcc, s[2:3]
	s_bcnt1_i32_b64 s59, vcc
	s_lshl_b32 s2, s59, 2
	s_add_i32 s2, s2, 0
	s_add_i32 s3, s2, 0x20484
	s_add_i32 s2, s2, 0x20400
	v_mov_b32_e32 v2, s3
	v_mov_b32_e32 v3, s2
	ds_read_b32 v4, v2
	ds_read2_b32 v[2:3], v3 offset1:1
	s_waitcnt lgkmcnt(0)
	v_lshlrev_b32_e32 v4, 4, v4
	v_sub_u32_e32 v3, v3, v2
	v_sub_u32_e32 v2, s22, v4
	s_branch .LBB0_779
.LBB0_773:
	s_cbranch_execz .LBB0_779
	s_mov_b32 s22, s23
	s_mov_b32 s24, 0
	s_mov_b32 s25, 0
	s_mov_b32 s26, 0
	s_mov_b64 s[2:3], exec
	s_mov_b64 exec, -1
	v_and_b32_e32 v2, 63, v0
	v_lshlrev_b32_e32 v2, 2, v2
	v_add_u32_e32 v2, 0x20400, v2
	ds_read_b32 v2, v2
	s_waitcnt lgkmcnt(0)
	v_lshlrev_b32_e32 v2, 4, v2
	v_cmp_ge_i32_e32 vcc, s23, v2
	s_mov_b64 exec, s[2:3]
	s_mov_b32 s2, 0xfffffffe
	s_mov_b32 s3, 0
	s_and_b64 vcc, vcc, s[2:3]
	s_bcnt1_i32_b64 s59, vcc
	s_lshl_b32 s2, s59, 2
	s_add_i32 s2, s2, 0
	s_add_i32 s2, s2, 0x20400
	v_mov_b32_e32 v2, s2
	ds_read2_b32 v[2:3], v2 offset1:1
	s_waitcnt lgkmcnt(0)
	v_readfirstlane_b32 s2, v2
	v_readfirstlane_b32 s3, v3
	s_sub_i32 s3, s3, s2
	s_abs_i32 s22, s3
	v_cvt_f32_u32_e32 v2, s22
	s_sub_i32 s25, 0, s22
	s_lshl_b32 s2, s2, 4
	s_sub_i32 s2, s23, s2
	v_rcp_iflag_f32_e32 v2, v2
	s_abs_i32 s24, s2
	s_xor_b32 s23, s2, s3
	s_ashr_i32 s23, s23, 31
	v_mul_f32_e32 v2, 0x4f7ffffe, v2
	v_cvt_u32_f32_e32 v2, v2
	s_nop 0
	v_readfirstlane_b32 s26, v2
	s_mul_i32 s25, s25, s26
	s_mul_hi_u32 s25, s26, s25
	s_add_i32 s26, s26, s25
	s_mul_hi_u32 s25, s24, s26
	s_mul_i32 s26, s25, s22
	s_sub_i32 s24, s24, s26
	s_add_i32 s27, s25, 1
	s_sub_i32 s26, s24, s22
	s_cmp_ge_u32 s24, s22
	s_cselect_b32 s25, s27, s25
	s_cselect_b32 s24, s26, s24
	s_add_i32 s26, s25, 1
	s_cmp_ge_u32 s24, s22
	s_cselect_b32 s22, s26, s25
	s_xor_b32 s22, s22, s23
	s_sub_i32 s22, s22, s23
	s_mul_i32 s3, s22, s3
	s_sub_i32 s2, s2, s3
	v_mov_b32_e32 v3, s2
	v_mov_b32_e32 v2, s22

; #define PG8_LAS __attribute__((address_space(3)))
; __device__ __forceinline__ unsigned long long rt() { return __builtin_amdgcn_s_memrealtime(); }
; #define AMP_BEGIN(k) unsigned long long amp_t0_ = 0; if ((PROBE_AMP >> (k)) & 1) amp_t0_ = __builtin_amdgcn_s_memrealtime()
;     __device__ __forceinline__ bool next(int i, Unit& u) const {
;         const PG8_LAS int* TH = TS + 33;
;         const int U = i * G + v; const int FT = __builtin_amdgcn_readfirstlane(TS[32] * nN), total = FT + __builtin_amdgcn_readfirstlane(TH[32] * nN); if (U >= total) return false;
;         int e = 0, pn, rt;
;         if (U < FT) {
; #pragma unroll 1
;             for (int j = 1; j < 32; ++j) e += (TS[j] * nN <= U) ? 1 : 0;
;             const int t0 = TS[e], nt = TS[e + 1] - t0, loc = U - t0 * nN; pn = loc / nt; rt = loc - pn * nt;
;         } else { const int U2 = U - FT;
; #pragma unroll 1
;             for (int j = 1; j < 32; ++j) e += (TH[j] * nN <= U2) ? 1 : 0;
;             pn = U2 - TH[e] * nN; rt = TS[e + 1] - TS[e]; }
; __global__ void __launch_bounds__(NWAVES * 64, 2) fwd(Args args) {
;     ...
;     if (IN(8)) for (int rep = 0; rep < REPS(8); ++rep) {
;         AMP_BEGIN(8);
;         {
;         pg8::GroupedOrder S{(const PG8_LAS int*)TS, (const PG8_LAS int*)CN, 8, G, vcu, (long)1024 * 2048 * 2, 256 * 2};
;         pg8::EpiFp8Y E{(unsigned char*)YB, 1.0f / (pg8::FP8_W_SCALE * pg8::FP8_ACT_SCALE), b_dn};
;         pg8::Gemm g{(const pg8::bf16_t*)ACT, (const pg8::bf16_t*)WDN, MAXSLOT, NE * 2048, DE / 2, 2048, 128 * 2};
;         pg8::gemm_phase<pg8::EpiFp8Y, pg8::GroupedOrder, true, true, true, true>(L, g, S, E); }
.LBB0_864:
	s_add_u32 s0, s36, 0x54000000
	s_addc_u32 s1, s37, 0
	s_cmp_lt_i32 s38, 9
	s_cselect_b64 s[2:3], -1, 0
	s_cmp_gt_i32 s39, 8
	s_cselect_b64 s[4:5], -1, 0
	s_and_b64 s[2:3], s[2:3], s[4:5]
	s_andn2_b64 vcc, exec, s[2:3]
	s_cbranch_vccnz .LBB0_967
	s_add_i32 s2, 0, 0x20480
	v_mov_b32_e32 v2, s2
	s_add_i32 s2, 0, 0x20504
	v_mov_b32_e32 v1, 0x7f7f7f7f
	v_mov_b32_e32 v3, s2
	ds_read_b32 v2, v2
	ds_read_b32 v3, v3
	v_readfirstlane_b32 s14, v0
	s_waitcnt lgkmcnt(1)
	v_readfirstlane_b32 s2, v2
	s_waitcnt lgkmcnt(0)
	v_readfirstlane_b32 s3, v3
	s_add_i32 s3, s3, s2
	s_lshl_b32 s3, s3, 3
	s_cmp_lt_i32 s29, s3
	s_cselect_b64 s[4:5], -1, 0
	s_cmp_ge_i32 s29, s3
	s_cbranch_scc1 .LBB0_872
	s_lshl_b32 s2, s2, 3
	s_cmp_ge_i32 s29, s2
	s_cbranch_scc0 .LBB0_873
	s_sub_i32 s8, s29, s2
	s_mov_b32 s9, s8
	s_mov_b32 s10, 0
	s_mov_b32 s11, 0
	s_mov_b32 s12, 0
	s_mov_b64 s[2:3], exec
	s_mov_b64 exec, -1
	v_and_b32_e32 v2, 63, v0
	v_lshlrev_b32_e32 v2, 2, v2
	v_add_u32_e32 v2, 0x20484, v2
	ds_read_b32 v2, v2
	s_waitcnt lgkmcnt(0)
	v_lshlrev_b32_e32 v2, 3, v2
	v_cmp_ge_i32_e32 vcc, s8, v2
	s_mov_b64 exec, s[2:3]
	s_mov_b32 s2, 0xfffffffe
	s_mov_b32 s3, 0
	s_and_b64 vcc, vcc, s[2:3]
	s_bcnt1_i32_b64 s42, vcc
	s_lshl_b32 s2, s42, 2
	s_add_i32 s2, s2, 0
	s_add_i32 s3, s2, 0x20484
	s_add_i32 s2, s2, 0x20400
	v_mov_b32_e32 v2, s3
	v_mov_b32_e32 v3, s2
	ds_read_b32 v4, v2
	ds_read2_b32 v[2:3], v3 offset1:1
	s_waitcnt lgkmcnt(1)
	v_lshlrev_b32_e32 v4, 3, v4
	s_waitcnt lgkmcnt(0)
	v_sub_u32_e32 v3, v3, v2
	v_sub_u32_e32 v2, s8, v4
	s_branch .LBB0_879

; __device__ __forceinline__ unsigned long long rt() { return __builtin_amdgcn_s_memrealtime(); }
;     __device__ __forceinline__ bool next(int i, Unit& u) const {
;     ...
;         if (U < FT) {
; #pragma unroll 1
;             for (int j = 1; j < 32; ++j) e += (TS[j] * nN <= U) ? 1 : 0;
;             const int t0 = TS[e], nt = TS[e + 1] - t0, loc = U - t0 * nN; pn = loc / nt; rt = loc - pn * nt;
;         } else { const int U2 = U - FT;
; #pragma unroll 1
;             for (int j = 1; j < 32; ++j) e += (TH[j] * nN <= U2) ? 1 : 0;
;             pn = U2 - TH[e] * nN; rt = TS[e + 1] - TS[e]; }
;         const int left = CN[e] - rt * BM;
.LBB0_873:
	s_cbranch_execz .LBB0_879
	s_mov_b32 s8, s29
	s_mov_b32 s9, 0
	s_mov_b32 s10, 0
	s_mov_b32 s11, 0
	s_mov_b64 s[2:3], exec
	s_mov_b64 exec, -1
	v_and_b32_e32 v2, 63, v0
	v_lshlrev_b32_e32 v2, 2, v2
	v_add_u32_e32 v2, 0x20400, v2
	ds_read_b32 v2, v2
	s_waitcnt lgkmcnt(0)
	v_lshlrev_b32_e32 v2, 3, v2
	v_cmp_ge_i32_e32 vcc, s29, v2
	s_mov_b64 exec, s[2:3]
	s_mov_b32 s2, 0xfffffffe
	s_mov_b32 s3, 0
	s_and_b64 vcc, vcc, s[2:3]
	s_bcnt1_i32_b64 s42, vcc
	s_lshl_b32 s2, s42, 2
	s_add_i32 s2, s2, 0
	s_add_i32 s2, s2, 0x20400
	v_mov_b32_e32 v2, s2
	ds_read2_b32 v[2:3], v2 offset1:1
	s_waitcnt lgkmcnt(0)
	v_readfirstlane_b32 s2, v2
	v_readfirstlane_b32 s3, v3
	s_sub_i32 s3, s3, s2
	s_abs_i32 s8, s3
	v_cvt_f32_u32_e32 v2, s8
	s_sub_i32 s11, 0, s8
	s_lshl_b32 s2, s2, 3
	s_sub_i32 s2, s29, s2
	v_rcp_iflag_f32_e32 v2, v2
	s_abs_i32 s10, s2
	s_xor_b32 s9, s2, s3
	s_ashr_i32 s9, s9, 31
	v_mul_f32_e32 v2, 0x4f7ffffe, v2
	v_cvt_u32_f32_e32 v2, v2
	s_nop 0
	v_readfirstlane_b32 s12, v2
	s_mul_i32 s11, s11, s12
	s_mul_hi_u32 s11, s12, s11
	s_add_i32 s12, s12, s11
	s_mul_hi_u32 s11, s10, s12
	s_mul_i32 s12, s11, s8
	s_sub_i32 s10, s10, s12
	s_add_i32 s13, s11, 1
	s_sub_i32 s12, s10, s8
	s_cmp_ge_u32 s10, s8
	s_cselect_b32 s11, s13, s11
	s_cselect_b32 s10, s12, s10
	s_add_i32 s12, s11, 1
	s_cmp_ge_u32 s10, s8
	s_cselect_b32 s8, s12, s11
	s_xor_b32 s8, s8, s9
	s_sub_i32 s8, s8, s9
	s_mul_i32 s3, s8, s3
	s_sub_i32 s2, s2, s3
	v_mov_b32_e32 v3, s2
	v_mov_b32_e32 v2, s8

; #define PG8_LAS __attribute__((address_space(3)))
; __device__ __forceinline__ unsigned long long rt() { return __builtin_amdgcn_s_memrealtime(); }
;     __device__ __forceinline__ bool next(int i, Unit& u) const {
;         const PG8_LAS int* TH = TS + 33;
;         const int U = i * G + v; const int FT = __builtin_amdgcn_readfirstlane(TS[32] * nN), total = FT + __builtin_amdgcn_readfirstlane(TH[32] * nN); if (U >= total) return false;
;         int e = 0, pn, rt;
;         if (U < FT) {
; #pragma unroll 1
;             for (int j = 1; j < 32; ++j) e += (TS[j] * nN <= U) ? 1 : 0;
;             const int t0 = TS[e], nt = TS[e + 1] - t0, loc = U - t0 * nN; pn = loc / nt; rt = loc - pn * nt;
;         } else { const int U2 = U - FT;
; #pragma unroll 1
;             for (int j = 1; j < 32; ++j) e += (TH[j] * nN <= U2) ? 1 : 0;
;             pn = U2 - TH[e] * nN; rt = TS[e + 1] - TS[e]; }
;         const int left = CN[e] - rt * BM;
;         u.pm = __builtin_amdgcn_readfirstlane(e * 32 + rt); u.pn = __builtin_amdgcn_readfirstlane(e * nN + pn); u.e = __builtin_amdgcn_readfirstlane(e); u.cn = __builtin_amdgcn_readfirstlane(pn);
;         u.rows = __builtin_amdgcn_readfirstlane(left < BM ? left : BM); u.boff = (long)u.e * b_estride + (long)u.cn * b_cnstep; return true;
.LBB0_885:
	ds_read_b32 v2, v221
	ds_read_b32 v3, v222
	s_add_i32 s61, s61, 1
	v_readlane_b32 s2, v251, 2
	s_mul_i32 s2, s61, s2
	s_add_i32 s29, s2, s29
	s_waitcnt lgkmcnt(0)
	v_readfirstlane_b32 s2, v2
	v_readfirstlane_b32 s3, v3
	s_add_i32 s3, s3, s2
	s_lshl_b32 s3, s3, 3
	s_cmp_lt_i32 s29, s3
	s_cselect_b64 s[26:27], -1, 0
	s_cmp_ge_i32 s29, s3
	s_cbranch_scc1 .LBB0_899
	s_lshl_b32 s2, s2, 3
	s_cmp_ge_i32 s29, s2
	s_cbranch_scc0 .LBB0_892
	s_sub_i32 s30, s29, s2
	s_mov_b32 s28, s30
	s_mov_b32 s31, 0
	s_mov_b32 s34, 0
	s_mov_b32 s35, 0
	s_mov_b64 s[2:3], exec
	s_mov_b64 exec, -1
	v_and_b32_e32 v2, 63, v0
	v_lshlrev_b32_e32 v2, 2, v2
	v_add_u32_e32 v2, 0x20484, v2
	ds_read_b32 v2, v2
	s_waitcnt lgkmcnt(0)
	v_lshlrev_b32_e32 v2, 3, v2
	v_cmp_ge_i32_e32 vcc, s30, v2
	s_mov_b64 exec, s[2:3]
	s_mov_b32 s2, 0xfffffffe
	s_mov_b32 s3, 0
	s_and_b64 vcc, vcc, s[2:3]
	s_bcnt1_i32_b64 s28, vcc
	s_lshl_b32 s2, s28, 2
	s_add_i32 s2, s2, 0
	s_add_i32 s3, s2, 0x20484
	s_add_i32 s2, s2, 0x20400
	v_mov_b32_e32 v2, s3
	v_mov_b32_e32 v3, s2
	ds_read_b32 v4, v2
	ds_read2_b32 v[2:3], v3 offset1:1
	s_waitcnt lgkmcnt(0)
	v_lshlrev_b32_e32 v4, 3, v4
	v_sub_u32_e32 v3, v3, v2
	v_sub_u32_e32 v2, s30, v4
	s_branch .LBB0_898
.LBB0_892:
	s_cbranch_execz .LBB0_898
	s_mov_b32 s28, s29
	s_mov_b32 s30, 0
	s_mov_b32 s31, 0
	s_mov_b32 s34, 0
	s_mov_b64 s[2:3], exec
	s_mov_b64 exec, -1
	v_and_b32_e32 v2, 63, v0
	v_lshlrev_b32_e32 v2, 2, v2
	v_add_u32_e32 v2, 0x20400, v2
	ds_read_b32 v2, v2
	s_waitcnt lgkmcnt(0)
	v_lshlrev_b32_e32 v2, 3, v2
	v_cmp_ge_i32_e32 vcc, s29, v2
	s_mov_b64 exec, s[2:3]
	s_mov_b32 s2, 0xfffffffe
	s_mov_b32 s3, 0
	s_and_b64 vcc, vcc, s[2:3]
	s_bcnt1_i32_b64 s28, vcc
	s_lshl_b32 s2, s28, 2
	s_add_i32 s2, s2, 0
	s_add_i32 s2, s2, 0x20400
	v_mov_b32_e32 v2, s2
	ds_read2_b32 v[2:3], v2 offset1:1
	s_waitcnt lgkmcnt(0)
	v_readfirstlane_b32 s2, v2
	v_readfirstlane_b32 s3, v3
	s_sub_i32 s3, s3, s2
	s_abs_i32 s30, s3
	v_cvt_f32_u32_e32 v2, s30
	s_sub_i32 s34, 0, s30
	s_lshl_b32 s2, s2, 3
	s_sub_i32 s2, s29, s2
	v_rcp_iflag_f32_e32 v2, v2
	s_abs_i32 s31, s2
	s_xor_b32 s29, s2, s3
	s_ashr_i32 s29, s29, 31
	v_mul_f32_e32 v2, 0x4f7ffffe, v2
	v_cvt_u32_f32_e32 v2, v2
	s_nop 0
	v_readfirstlane_b32 s35, v2
	s_mul_i32 s34, s34, s35
	s_mul_hi_u32 s34, s35, s34
	s_add_i32 s35, s35, s34
	s_mul_hi_u32 s34, s31, s35
	s_mul_i32 s35, s34, s30
	s_sub_i32 s31, s31, s35
	s_add_i32 s36, s34, 1
	s_sub_i32 s35, s31, s30
	s_cmp_ge_u32 s31, s30
	s_cselect_b32 s34, s36, s34
	s_cselect_b32 s31, s35, s31
	s_add_i32 s35, s34, 1
	s_cmp_ge_u32 s31, s30
	s_cselect_b32 s30, s35, s34
	s_xor_b32 s30, s30, s29
	s_sub_i32 s29, s30, s29
	s_mul_i32 s3, s29, s3
	s_sub_i32 s2, s2, s3
	v_mov_b32_e32 v3, s2
	v_mov_b32_e32 v2, s29

.LBB0_901:
	ds_read_b64_tr_b16 v[26:27], v207 offset:0
	ds_read_b64_tr_b16 v[28:29], v207 offset:1024
	ds_read_b64_tr_b16 v[30:31], v207 offset:8192
	ds_read_b64_tr_b16 v[32:33], v207 offset:9216
	ds_read_b64_tr_b16 v[18:19], v217 offset:0
	ds_read_b64_tr_b16 v[20:21], v217 offset:1024
	ds_read_b64_tr_b16 v[22:23], v217 offset:8192
	ds_read_b64_tr_b16 v[24:25], v217 offset:9216
	ds_read_b64_tr_b16 v[10:11], v214 offset:0
	ds_read_b64_tr_b16 v[12:13], v214 offset:1024
	ds_read_b64_tr_b16 v[14:15], v214 offset:8192
	ds_read_b64_tr_b16 v[16:17], v214 offset:9216
	ds_read_b64_tr_b16 v[2:3], v218 offset:0
	ds_read_b64_tr_b16 v[4:5], v218 offset:1024
	ds_read_b64_tr_b16 v[6:7], v218 offset:8192
	ds_read_b64_tr_b16 v[8:9], v218 offset:9216
	s_add_u32 s2, s50, 0xfffc0080
	s_addc_u32 s3, s51, -1
	s_cmp_eq_u32 s72, 12
	s_cselect_b32 s55, s29, s3
	s_cselect_b32 s54, s31, s2
	s_cselect_b32 s53, s35, s71
	s_cselect_b32 s52, s43, s70
	ds_read_b128 v[34:37], v223
	ds_read_b128 v[38:41], v223 offset:1024
	ds_read_b128 v[42:45], v223 offset:2048
	ds_read_b128 v[46:49], v223 offset:3072
	ds_read_b128 v[50:53], v223 offset:4096
	ds_read_b128 v[54:57], v223 offset:5120
	ds_read_b128 v[58:61], v223 offset:6144
	ds_read_b128 v[62:65], v223 offset:7168
	s_waitcnt vmcnt(6)
	s_waitcnt lgkmcnt(0)
	s_barrier
	s_setprio 1
	s_waitcnt lgkmcnt(0)
	v_mfma_scale_f32_16x16x128_f8f6f4 v[194:197], v[26:33], v[34:41], v[194:197], v1, v1 op_sel_hi:[0,0,0]
	v_mfma_scale_f32_16x16x128_f8f6f4 v[190:193], v[18:25], v[34:41], v[190:193], v1, v1 op_sel_hi:[0,0,0]
	v_mfma_scale_f32_16x16x128_f8f6f4 v[186:189], v[26:33], v[42:49], v[186:189], v1, v1 op_sel_hi:[0,0,0]
	v_mfma_scale_f32_16x16x128_f8f6f4 v[182:185], v[18:25], v[42:49], v[182:185], v1, v1 op_sel_hi:[0,0,0]
	v_lshl_add_u64 v[68:69], s[50:51], 0, v[208:209]
	s_add_i32 m0, s17, 0xc000
	s_nop 0
	global_load_lds_dwordx4 v[68:69], off
	v_mfma_scale_f32_16x16x128_f8f6f4 v[162:165], v[26:33], v[50:57], v[162:165], v1, v1 op_sel_hi:[0,0,0]
	v_mfma_scale_f32_16x16x128_f8f6f4 v[158:161], v[18:25], v[50:57], v[158:161], v1, v1 op_sel_hi:[0,0,0]
	v_mfma_scale_f32_16x16x128_f8f6f4 v[146:149], v[26:33], v[58:65], v[146:149], v1, v1 op_sel_hi:[0,0,0]
	v_mfma_scale_f32_16x16x128_f8f6f4 v[142:145], v[18:25], v[58:65], v[142:145], v1, v1 op_sel_hi:[0,0,0]
	s_setprio 0
	s_setprio 1
	v_mfma_scale_f32_16x16x128_f8f6f4 v[178:181], v[10:17], v[34:41], v[178:181], v1, v1 op_sel_hi:[0,0,0]
	v_mfma_scale_f32_16x16x128_f8f6f4 v[174:177], v[2:9], v[34:41], v[174:177], v1, v1 op_sel_hi:[0,0,0]
	v_lshl_add_u64 v[68:69], s[50:51], 0, v[210:211]
	s_add_i32 m0, s17, 0xe000
	s_nop 0
	global_load_lds_dwordx4 v[68:69], off
	v_mfma_scale_f32_16x16x128_f8f6f4 v[170:173], v[10:17], v[42:49], v[170:173], v1, v1 op_sel_hi:[0,0,0]
	v_mfma_scale_f32_16x16x128_f8f6f4 v[166:169], v[2:9], v[42:49], v[166:169], v1, v1 op_sel_hi:[0,0,0]
	v_mfma_scale_f32_16x16x128_f8f6f4 v[154:157], v[10:17], v[50:57], v[154:157], v1, v1 op_sel_hi:[0,0,0]
	v_mfma_scale_f32_16x16x128_f8f6f4 v[150:153], v[2:9], v[50:57], v[150:153], v1, v1 op_sel_hi:[0,0,0]
	v_mfma_scale_f32_16x16x128_f8f6f4 v[138:141], v[10:17], v[58:65], v[138:141], v1, v1 op_sel_hi:[0,0,0]
	v_mfma_scale_f32_16x16x128_f8f6f4 v[134:137], v[2:9], v[58:65], v[134:137], v1, v1 op_sel_hi:[0,0,0]
	s_setprio 0
	s_barrier
	ds_read_b128 v[58:61], v223 offset:16384
	ds_read_b128 v[62:65], v223 offset:17408
	ds_read_b128 v[50:53], v223 offset:18432
	ds_read_b128 v[54:57], v223 offset:19456
	ds_read_b128 v[42:45], v223 offset:20480
	ds_read_b128 v[46:49], v223 offset:21504
	ds_read_b128 v[34:37], v223 offset:22528
	ds_read_b128 v[38:41], v223 offset:23552
	v_cmp_ne_u32_e64 s[2:3], 1, v225
	s_andn2_b64 vcc, exec, s[48:49]
	s_waitcnt vmcnt(2)
	s_waitcnt lgkmcnt(0)
	s_barrier
	s_cbranch_vccnz .Lp8_skip_b
	s_setprio 1
	s_waitcnt lgkmcnt(0)
	v_mfma_scale_f32_16x16x128_f8f6f4 v[130:133], v[26:33], v[58:65], v[130:133], v1, v1 op_sel_hi:[0,0,0]
	v_mfma_scale_f32_16x16x128_f8f6f4 v[126:129], v[18:25], v[58:65], v[126:129], v1, v1 op_sel_hi:[0,0,0]
	s_mov_b32 m0, s19
	v_lshl_add_u64 v[68:69], s[52:53], 0, v[200:201]
	global_load_lds_dwordx4 v[68:69], off
	v_mfma_scale_f32_16x16x128_f8f6f4 v[114:117], v[26:33], v[50:57], v[114:117], v1, v1 op_sel_hi:[0,0,0]
	v_mfma_scale_f32_16x16x128_f8f6f4 v[110:113], v[18:25], v[50:57], v[110:113], v1, v1 op_sel_hi:[0,0,0]
	v_lshl_add_u64 v[212:213], s[52:53], 0, v[204:205]
	s_mov_b32 m0, s33
	v_lshl_add_u64 v[68:69], v[68:69], 0, s[4:5]
	global_load_lds_dwordx4 v[212:213], off
	v_mfma_scale_f32_16x16x128_f8f6f4 v[98:101], v[26:33], v[42:49], v[98:101], v1, v1 op_sel_hi:[0,0,0]
	v_mfma_scale_f32_16x16x128_f8f6f4 v[94:97], v[18:25], v[42:49], v[94:97], v1, v1 op_sel_hi:[0,0,0]
	s_mov_b32 m0, s45
	s_nop 0
	global_load_lds_dwordx4 v[68:69], off
	v_mfma_scale_f32_16x16x128_f8f6f4 v[82:85], v[26:33], v[34:41], v[82:85], v1, v1 op_sel_hi:[0,0,0]
	v_mfma_scale_f32_16x16x128_f8f6f4 v[78:81], v[18:25], v[34:41], v[78:81], v1, v1 op_sel_hi:[0,0,0]
	s_setprio 0
	s_setprio 1
	v_mfma_scale_f32_16x16x128_f8f6f4 v[122:125], v[10:17], v[58:65], v[122:125], v1, v1 op_sel_hi:[0,0,0]
	v_lshl_add_u64 v[68:69], v[212:213], 0, s[4:5]
	s_mov_b32 m0, s47
	v_lshl_add_u64 v[212:213], s[54:55], 0, v[202:203]
	global_load_lds_dwordx4 v[68:69], off
	v_mfma_scale_f32_16x16x128_f8f6f4 v[118:121], v[2:9], v[58:65], v[118:121], v1, v1 op_sel_hi:[0,0,0]
	v_mfma_scale_f32_16x16x128_f8f6f4 v[106:109], v[10:17], v[50:57], v[106:109], v1, v1 op_sel_hi:[0,0,0]
	v_lshl_add_u64 v[68:69], s[54:55], 0, v[198:199]
	s_mov_b32 m0, s17
	s_nop 0
	global_load_lds_dwordx4 v[68:69], off
	v_mfma_scale_f32_16x16x128_f8f6f4 v[102:105], v[2:9], v[50:57], v[102:105], v1, v1 op_sel_hi:[0,0,0]
	v_mfma_scale_f32_16x16x128_f8f6f4 v[90:93], v[10:17], v[42:49], v[90:93], v1, v1 op_sel_hi:[0,0,0]
	s_mov_b32 m0, s58
	s_nop 0
	global_load_lds_dwordx4 v[212:213], off
	v_mfma_scale_f32_16x16x128_f8f6f4 v[86:89], v[2:9], v[42:49], v[86:89], v1, v1 op_sel_hi:[0,0,0]
	v_mfma_scale_f32_16x16x128_f8f6f4 v[74:77], v[10:17], v[34:41], v[74:77], v1, v1 op_sel_hi:[0,0,0]
	v_mfma_scale_f32_16x16x128_f8f6f4 v[70:73], v[2:9], v[34:41], v[70:73], v1, v1 op_sel_hi:[0,0,0]
	s_setprio 0
.LBB0_903:
	s_add_u32 s56, s52, 0x40000
	s_addc_u32 s57, s53, 0
	s_barrier
	ds_read_b64_tr_b16 v[26:27], v215 offset:0
	ds_read_b64_tr_b16 v[28:29], v215 offset:1024
	ds_read_b64_tr_b16 v[30:31], v215 offset:8192
	ds_read_b64_tr_b16 v[32:33], v215 offset:9216
	ds_read_b64_tr_b16 v[18:19], v219 offset:0
	ds_read_b64_tr_b16 v[20:21], v219 offset:1024
	ds_read_b64_tr_b16 v[22:23], v219 offset:8192
	ds_read_b64_tr_b16 v[24:25], v219 offset:9216
	ds_read_b64_tr_b16 v[10:11], v216 offset:0
	ds_read_b64_tr_b16 v[12:13], v216 offset:1024
	ds_read_b64_tr_b16 v[14:15], v216 offset:8192
	ds_read_b64_tr_b16 v[16:17], v216 offset:9216
	ds_read_b64_tr_b16 v[2:3], v220 offset:0
	ds_read_b64_tr_b16 v[4:5], v220 offset:1024
	ds_read_b64_tr_b16 v[6:7], v220 offset:8192
	ds_read_b64_tr_b16 v[8:9], v220 offset:9216
	s_add_u32 s54, s54, 0x40000
	s_addc_u32 s55, s55, 0
	ds_read_b128 v[34:37], v223 offset:32768
	ds_read_b128 v[38:41], v223 offset:33792
	ds_read_b128 v[42:45], v223 offset:34816
	ds_read_b128 v[46:49], v223 offset:35840
	ds_read_b128 v[50:53], v223 offset:36864
	ds_read_b128 v[54:57], v223 offset:37888
	ds_read_b128 v[58:61], v223 offset:38912
	ds_read_b128 v[62:65], v223 offset:39936
	s_waitcnt vmcnt(6)
	s_waitcnt lgkmcnt(0)
	s_barrier
	s_setprio 1
	s_waitcnt lgkmcnt(0)
	v_mfma_scale_f32_16x16x128_f8f6f4 v[194:197], v[26:33], v[34:41], v[194:197], v1, v1 op_sel_hi:[0,0,0]
	v_mfma_scale_f32_16x16x128_f8f6f4 v[190:193], v[18:25], v[34:41], v[190:193], v1, v1 op_sel_hi:[0,0,0]
	v_mfma_scale_f32_16x16x128_f8f6f4 v[186:189], v[26:33], v[42:49], v[186:189], v1, v1 op_sel_hi:[0,0,0]
	v_mfma_scale_f32_16x16x128_f8f6f4 v[182:185], v[18:25], v[42:49], v[182:185], v1, v1 op_sel_hi:[0,0,0]
	s_mov_b32 m0, s59
	v_lshl_add_u64 v[226:227], s[54:55], 0, v[198:199]
	global_load_lds_dwordx4 v[226:227], off
	v_mfma_scale_f32_16x16x128_f8f6f4 v[162:165], v[26:33], v[50:57], v[162:165], v1, v1 op_sel_hi:[0,0,0]
	v_mfma_scale_f32_16x16x128_f8f6f4 v[158:161], v[18:25], v[50:57], v[158:161], v1, v1 op_sel_hi:[0,0,0]
	v_mfma_scale_f32_16x16x128_f8f6f4 v[146:149], v[26:33], v[58:65], v[146:149], v1, v1 op_sel_hi:[0,0,0]
	v_mfma_scale_f32_16x16x128_f8f6f4 v[142:145], v[18:25], v[58:65], v[142:145], v1, v1 op_sel_hi:[0,0,0]
	s_setprio 0
	s_setprio 1
	v_mfma_scale_f32_16x16x128_f8f6f4 v[178:181], v[10:17], v[34:41], v[178:181], v1, v1 op_sel_hi:[0,0,0]
	v_mfma_scale_f32_16x16x128_f8f6f4 v[174:177], v[2:9], v[34:41], v[174:177], v1, v1 op_sel_hi:[0,0,0]
	v_lshl_add_u64 v[226:227], s[54:55], 0, v[202:203]
	s_mov_b32 m0, s60
	s_nop 0
	global_load_lds_dwordx4 v[226:227], off
	v_mfma_scale_f32_16x16x128_f8f6f4 v[170:173], v[10:17], v[42:49], v[170:173], v1, v1 op_sel_hi:[0,0,0]
	v_mfma_scale_f32_16x16x128_f8f6f4 v[166:169], v[2:9], v[42:49], v[166:169], v1, v1 op_sel_hi:[0,0,0]
	v_mfma_scale_f32_16x16x128_f8f6f4 v[154:157], v[10:17], v[50:57], v[154:157], v1, v1 op_sel_hi:[0,0,0]
	v_mfma_scale_f32_16x16x128_f8f6f4 v[150:153], v[2:9], v[50:57], v[150:153], v1, v1 op_sel_hi:[0,0,0]
	v_mfma_scale_f32_16x16x128_f8f6f4 v[138:141], v[10:17], v[58:65], v[138:141], v1, v1 op_sel_hi:[0,0,0]
	v_mfma_scale_f32_16x16x128_f8f6f4 v[134:137], v[2:9], v[58:65], v[134:137], v1, v1 op_sel_hi:[0,0,0]
	s_setprio 0
	s_barrier
	ds_read_b128 v[58:61], v223 offset:49152
	ds_read_b128 v[62:65], v223 offset:50176
	ds_read_b128 v[50:53], v223 offset:51200
	ds_read_b128 v[54:57], v223 offset:52224
	ds_read_b128 v[42:45], v223 offset:53248
	ds_read_b128 v[46:49], v223 offset:54272
	ds_read_b128 v[34:37], v223 offset:55296
	ds_read_b128 v[38:41], v223 offset:56320
	s_and_b64 vcc, exec, s[2:3]
	s_waitcnt vmcnt(2)
	s_waitcnt lgkmcnt(0)
	s_barrier
	s_cbranch_vccnz .Lp8_skip_d
	s_setprio 1
	s_waitcnt lgkmcnt(0)
	v_mfma_scale_f32_16x16x128_f8f6f4 v[130:133], v[26:33], v[58:65], v[130:133], v1, v1 op_sel_hi:[0,0,0]
	v_mfma_scale_f32_16x16x128_f8f6f4 v[126:129], v[18:25], v[58:65], v[126:129], v1, v1 op_sel_hi:[0,0,0]
	v_lshl_add_u64 v[226:227], s[56:57], 0, v[200:201]
	s_add_i32 m0, s17, 0x18000
	s_nop 0
	global_load_lds_dwordx4 v[226:227], off
	v_mfma_scale_f32_16x16x128_f8f6f4 v[114:117], v[26:33], v[50:57], v[114:117], v1, v1 op_sel_hi:[0,0,0]
	v_mfma_scale_f32_16x16x128_f8f6f4 v[110:113], v[18:25], v[50:57], v[110:113], v1, v1 op_sel_hi:[0,0,0]
	s_add_i32 m0, s17, 0x1a000
	v_lshl_add_u64 v[226:227], s[56:57], 0, v[204:205]
	global_load_lds_dwordx4 v[226:227], off
	v_mfma_scale_f32_16x16x128_f8f6f4 v[98:101], v[26:33], v[42:49], v[98:101], v1, v1 op_sel_hi:[0,0,0]
	v_mfma_scale_f32_16x16x128_f8f6f4 v[94:97], v[18:25], v[42:49], v[94:97], v1, v1 op_sel_hi:[0,0,0]
	s_add_u32 s52, s52, 0x40100
	s_addc_u32 s53, s53, 0
	v_lshl_add_u64 v[226:227], s[52:53], 0, v[200:201]
	s_add_i32 m0, s17, 0x1c000
	v_lshl_add_u64 v[68:69], v[68:69], 0, s[12:13]
	global_load_lds_dwordx4 v[226:227], off
	v_mfma_scale_f32_16x16x128_f8f6f4 v[82:85], v[26:33], v[34:41], v[82:85], v1, v1 op_sel_hi:[0,0,0]
	v_mfma_scale_f32_16x16x128_f8f6f4 v[78:81], v[18:25], v[34:41], v[78:81], v1, v1 op_sel_hi:[0,0,0]
	s_setprio 0
	s_setprio 1
	v_mfma_scale_f32_16x16x128_f8f6f4 v[122:125], v[10:17], v[58:65], v[122:125], v1, v1 op_sel_hi:[0,0,0]
	v_lshl_add_u64 v[226:227], s[52:53], 0, v[204:205]
	s_add_i32 m0, s17, 0x1e000
	s_nop 0
	global_load_lds_dwordx4 v[226:227], off
	v_mfma_scale_f32_16x16x128_f8f6f4 v[118:121], v[2:9], v[58:65], v[118:121], v1, v1 op_sel_hi:[0,0,0]
	v_mfma_scale_f32_16x16x128_f8f6f4 v[106:109], v[10:17], v[50:57], v[106:109], v1, v1 op_sel_hi:[0,0,0]
	s_mov_b32 m0, s62
	s_nop 0
	global_load_lds_dwordx4 v[68:69], off
	v_mfma_scale_f32_16x16x128_f8f6f4 v[102:105], v[2:9], v[50:57], v[102:105], v1, v1 op_sel_hi:[0,0,0]
	v_mfma_scale_f32_16x16x128_f8f6f4 v[90:93], v[10:17], v[42:49], v[90:93], v1, v1 op_sel_hi:[0,0,0]
	v_lshl_add_u64 v[68:69], v[212:213], 0, s[12:13]
	s_mov_b32 m0, s63
	s_nop 0
	global_load_lds_dwordx4 v[68:69], off
	v_mfma_scale_f32_16x16x128_f8f6f4 v[86:89], v[2:9], v[42:49], v[86:89], v1, v1 op_sel_hi:[0,0,0]
	v_mfma_scale_f32_16x16x128_f8f6f4 v[74:77], v[10:17], v[34:41], v[74:77], v1, v1 op_sel_hi:[0,0,0]
	v_mfma_scale_f32_16x16x128_f8f6f4 v[70:73], v[2:9], v[34:41], v[70:73], v1, v1 op_sel_hi:[0,0,0]
	s_setprio 0
	s_branch .LBB0_900
.Lp8_skip_b:
	s_mov_b32 m0, s19
	v_lshl_add_u64 v[68:69], s[52:53], 0, v[200:201]
	global_load_lds_dwordx4 v[68:69], off
	v_lshl_add_u64 v[212:213], s[52:53], 0, v[204:205]
	s_mov_b32 m0, s33
	v_lshl_add_u64 v[68:69], v[68:69], 0, s[4:5]
	global_load_lds_dwordx4 v[212:213], off
	s_mov_b32 m0, s45
	s_nop 0
	global_load_lds_dwordx4 v[68:69], off
	v_lshl_add_u64 v[68:69], v[212:213], 0, s[4:5]
	s_mov_b32 m0, s47
	v_lshl_add_u64 v[212:213], s[54:55], 0, v[202:203]
	global_load_lds_dwordx4 v[68:69], off
	v_lshl_add_u64 v[68:69], s[54:55], 0, v[198:199]
	s_mov_b32 m0, s17
	s_nop 0
	global_load_lds_dwordx4 v[68:69], off
	s_mov_b32 m0, s58
	s_nop 0
	global_load_lds_dwordx4 v[212:213], off
	s_branch .LBB0_903
.Lp8_skip_d:
	v_lshl_add_u64 v[226:227], s[56:57], 0, v[200:201]
	s_add_i32 m0, s17, 0x18000
	s_nop 0
	global_load_lds_dwordx4 v[226:227], off
	s_add_i32 m0, s17, 0x1a000
	v_lshl_add_u64 v[226:227], s[56:57], 0, v[204:205]
	global_load_lds_dwordx4 v[226:227], off
	s_add_u32 s52, s52, 0x40100
	s_addc_u32 s53, s53, 0
	v_lshl_add_u64 v[226:227], s[52:53], 0, v[200:201]
	s_add_i32 m0, s17, 0x1c000
	v_lshl_add_u64 v[68:69], v[68:69], 0, s[12:13]
	global_load_lds_dwordx4 v[226:227], off
	v_lshl_add_u64 v[226:227], s[52:53], 0, v[204:205]
	s_add_i32 m0, s17, 0x1e000
	s_nop 0
	global_load_lds_dwordx4 v[226:227], off
	s_mov_b32 m0, s62
	s_nop 0
	global_load_lds_dwordx4 v[68:69], off
	v_lshl_add_u64 v[68:69], v[212:213], 0, s[12:13]
	s_mov_b32 m0, s63
	s_nop 0
	global_load_lds_dwordx4 v[68:69], off
	s_branch .LBB0_900
